# MLA attention: conflict-free LDS swizzles for K nope (16-slot XOR) and K rope ((row>>1)&7) tiles, on top of final-phase rewrite
# speedup vs baseline: 1.0033x; 1.0033x over previous
.LBB0_939:
	v_mov_b32_e32 v194, v0
	s_or_b64 s[22:23], s[4:5], s[68:69]
	v_readfirstlane_b32 s0, v194
	s_ashr_i32 s18, s0, 6
	s_and_b64 s[12:13], s[2:3], exec
	s_cselect_b32 s1, s76, s77
	s_lshl_b32 s35, s18, 5
	s_or_b32 s12, s26, s1
	s_ashr_i32 s13, s35, 31
	s_add_u32 s12, s12, s35
	s_addc_u32 s13, s27, s13
	s_mul_i32 s16, s13, 0xc00
	s_mul_hi_u32 s17, s12, 0xc00
	v_and_b32_e32 v195, 31, v194
	v_bfe_u32 v196, v194, 5, 1
	s_add_i32 s17, s17, s16
	s_mul_i32 s16, s12, 0xc00
	s_add_u32 s16, s72, s16
	v_lshlrev_b32_e32 v20, 4, v196
	v_mul_u32_u24_e32 v1, 0xc00, v195
	s_addc_u32 s17, s73, s17
	v_or_b32_e32 v1, v20, v1
	global_load_dwordx4 v[130:133], v1, s[16:17]
	global_load_dwordx4 v[134:137], v1, s[16:17] offset:32
	global_load_dwordx4 v[138:141], v1, s[16:17] offset:64
	global_load_dwordx4 v[142:145], v1, s[16:17] offset:96
	global_load_dwordx4 v[146:149], v1, s[16:17] offset:128
	global_load_dwordx4 v[150:153], v1, s[16:17] offset:160
	global_load_dwordx4 v[154:157], v1, s[16:17] offset:192
	global_load_dwordx4 v[158:161], v1, s[16:17] offset:224
	global_load_dwordx4 v[162:165], v1, s[16:17] offset:256
	global_load_dwordx4 v[166:169], v1, s[16:17] offset:288
	global_load_dwordx4 v[170:173], v1, s[16:17] offset:320
	global_load_dwordx4 v[174:177], v1, s[16:17] offset:352
	s_lshl_b32 s16, s18, 3
	s_waitcnt lgkmcnt(0)
	v_bfe_u32 v3, v194, 2, 3
	v_mov_b32_e32 v4, 0xffff3
	v_bitop3_b32 v3, s16, v4, v3 bitop3:0xc8
	v_lshrrev_b32_e32 v4, 1, v194
	s_lshl_b32 s17, s18, 2
	v_bfe_u32 v1, v194, 4, 2
	v_lshlrev_b32_e32 v21, 4, v194
	v_and_b32_e32 v4, 8, v4
	s_and_b32 s17, s17, 4
	v_and_b32_e32 v6, 48, v194
	s_movk_i32 s19, 0xf0
	v_or3_b32 v3, v4, v3, s17
	s_lshl_b32 s17, s18, 15
	v_lshlrev_b32_e32 v5, 12, v1
	v_bitop3_b32 v6, v21, v6, s19 bitop3:0x6c
	s_lshl_b32 s21, s18, 7
	s_and_b32 s21, s21, 0x80
	v_xor_b32_e32 v6, s21, v6
	v_and_b32_e32 v4, 48, v21
	v_lshlrev_b32_e32 v3, 12, v3
	v_or3_b32 v198, s17, v5, v6
	v_lshlrev_b32_e32 v5, 6, v196
	v_or3_b32 v1, v1, s16, 4
	v_or3_b32 v3, v3, v4, v5
	v_lshlrev_b32_e32 v4, 12, v1
	v_lshlrev_b32_e32 v1, 4, v1
	v_and_b32_e32 v2, 0xf0, v21
	v_and_b32_e32 v1, 0xf0, v1
	v_bitop3_b32 v200, v1, v4, v2 bitop3:0xde
	v_bfe_u32 v1, v194, 3, 3
	v_lshlrev_b32_e32 v2, 7, v1
	v_bfe_u32 v4, v194, 4, 2
	s_and_b32 s21, s18, 1
	s_lshl_b32 s21, s21, 2
	v_or_b32_e32 v4, s21, v4
	v_bitop3_b32 v1, v4, v194, 7 bitop3:0x78
	s_lshl_b32 s16, s18, 10
	v_lshlrev_b32_e32 v1, 4, v1
	s_lshl_b32 s17, s18, 11
	v_or3_b32 v201, v1, v2, s16
	s_add_i32 s17, s17, 0
	s_add_i32 s16, s16, 0
	v_or_b32_e32 v197, 0x100, v3
	v_or_b32_e32 v199, 0x180, v3
	s_add_i32 s19, s17, 0xc000
	s_add_i32 s18, s16, 0x18000
	s_and_b64 vcc, exec, s[22:23]
	s_cbranch_vccnz .LBB0_941
	s_mov_b32 m0, s19
	s_nop 0
	global_load_lds_dwordx4 v198, s[38:39]
	s_add_i32 s21, s17, 0xc400
	s_mov_b32 m0, s21
	s_nop 0
	global_load_lds_dwordx4 v200, s[38:39]
	s_mov_b32 m0, s17
	s_nop 0
	global_load_lds_dwordx4 v197, s[38:39]
	s_add_i32 s21, s17, 0x400
	s_mov_b32 m0, s21
	s_nop 0
	global_load_lds_dwordx4 v199, s[38:39]
	s_mov_b32 m0, s18
	s_nop 0
	global_load_lds_dwordx4 v201, s[56:57]
	s_add_i32 s21, s17, 0x10000
	s_mov_b32 m0, s21
	s_nop 0
	global_load_lds_dwordx4 v198, s[58:59]
	s_add_i32 s21, s17, 0x10400
	s_mov_b32 m0, s21
	s_nop 0
	global_load_lds_dwordx4 v200, s[58:59]
	s_add_i32 s21, s17, 0x4000
	s_mov_b32 m0, s21
	s_nop 0
	global_load_lds_dwordx4 v197, s[58:59]
	s_add_i32 s21, s17, 0x4400
	s_mov_b32 m0, s21
	s_nop 0
	global_load_lds_dwordx4 v199, s[58:59]
	s_add_i32 s21, s16, 0x1a000
	s_mov_b32 m0, s21
	s_nop 0
	global_load_lds_dwordx4 v201, s[60:61]
.LBB0_941:
	v_and_b32_e32 v1, 63, v194
	v_lshlrev_b32_e32 v4, 4, v1
	v_lshlrev_b32_e32 v3, 3, v1
	v_and_b32_e32 v4, 0xc0, v4
	v_lshlrev_b32_e32 v5, 1, v1
	v_and_b32_e32 v2, 15, v194
	v_and_or_b32 v4, v3, 24, v4
	v_and_b32_e32 v5, 32, v5
	v_and_b32_e32 v3, 0x100, v3
	v_or3_b32 v19, v4, v5, v3
	v_lshlrev_b32_e32 v3, 8, v195
	v_xor_b32_e32 v2, v196, v2
	v_lshl_or_b32 v202, v2, 4, v3
	v_add_u32_e32 v30, 0, v202
	s_waitcnt vmcnt(0)
	s_waitcnt vmcnt(63) expcnt(7) lgkmcnt(15)
	s_barrier
	ds_read_b128 v[22:25], v30 offset:49152
	ds_read_b128 v[26:29], v30 offset:57344
	v_xor_b32_e32 v30, 0x80, v30
	v_and_b32_e32 v4, 0xf0, v21
	v_or_b32_e32 v2, 32, v20
	s_waitcnt vmcnt(11) lgkmcnt(1)
	v_mfma_f32_32x32x16_bf16 v[66:81], v[22:25], v[130:133], 0
	v_bitop3_b32 v207, v2, v3, v4 bitop3:0xde
	v_add_u32_e32 v31, 0, v207
	v_or_b32_e32 v2, 64, v20
	v_bitop3_b32 v209, v2, v3, v4 bitop3:0xde
	v_add_u32_e32 v32, 0, v209
	v_or_b32_e32 v2, 0x60, v20
	v_bitop3_b32 v224, v2, v3, v4 bitop3:0xde
	s_waitcnt lgkmcnt(0)
	v_mfma_f32_32x32x16_bf16 v[82:97], v[26:29], v[130:133], 0
	ds_read_b128 v[22:25], v31 offset:49152
	ds_read_b128 v[26:29], v31 offset:57344
	v_xor_b32_e32 v31, 0x80, v31
	v_add_u32_e32 v33, 0, v224
	s_xor_b64 s[66:67], s[2:3], -1
	s_add_i32 s2, s1, 0x100
	s_add_i32 s35, s35, s1
	s_add_i32 s1, 0, 0x18000
	v_lshl_add_u32 v225, v195, 7, s1
	s_waitcnt vmcnt(10) lgkmcnt(1)
	v_mfma_f32_32x32x16_bf16 v[66:81], v[22:25], v[134:137], v[66:81]
	s_movk_i32 s1, 0x70
	v_lshlrev_b32_e32 v4, 3, v194
	v_and_b32_e32 v4, 0x70, v4
	v_xor_b32_e32 v226, v20, v4
	v_bitop3_b32 v206, v20, v4, 32 bitop3:0x36
	v_bitop3_b32 v208, v20, v4, 64 bitop3:0x36
	v_bitop3_b32 v223, v20, v4, s94 bitop3:0x36
	s_and_b32 s0, s0, 0x3fffffc0
	s_lshl_b32 s0, s0, 2
	s_waitcnt lgkmcnt(0)
	v_mfma_f32_32x32x16_bf16 v[82:97], v[26:29], v[134:137], v[82:97]
	ds_read_b128 v[22:25], v32 offset:49152
	ds_read_b128 v[26:29], v32 offset:57344
	v_xor_b32_e32 v32, 0x80, v32
	s_add_i32 s0, s0, 0
	s_mov_b32 s40, 0
	s_add_i32 s0, s0, 0x1e000
	s_mov_b32 s41, s40
	s_lshr_b32 s21, s2, 6
	s_mov_b32 s42, s40
	s_waitcnt vmcnt(9) lgkmcnt(1)
	v_mfma_f32_32x32x16_bf16 v[66:81], v[22:25], v[138:141], v[66:81]
	s_mov_b32 s43, s40
	s_mov_b32 s44, s40
	s_mov_b32 s45, s40
	s_mov_b32 s46, s40
	s_mov_b32 s47, s40
	s_mov_b32 s48, s40
	s_mov_b32 s49, s40
	s_waitcnt lgkmcnt(0)
	v_mfma_f32_32x32x16_bf16 v[82:97], v[26:29], v[138:141], v[82:97]
	ds_read_b128 v[22:25], v33 offset:49152
	ds_read_b128 v[26:29], v33 offset:57344
	v_xor_b32_e32 v33, 0x80, v33
	s_mov_b32 s50, s40
	s_mov_b32 s51, s40
	s_mov_b32 s52, s40
	s_mov_b32 s53, s40
	s_mov_b32 s54, s40
	s_mov_b32 s55, s40
	s_waitcnt vmcnt(8) lgkmcnt(1)
	v_mfma_f32_32x32x16_bf16 v[66:81], v[22:25], v[142:145], v[66:81]
	v_mov_b64_e32 v[2:3], s[40:41]
	v_cmp_gt_u32_e64 s[2:3], 32, v1
	v_lshl_add_u32 v227, v195, 2, s0
	v_lshl_add_u32 v1, v196, 4, s0
	s_sub_i32 s0, s35, 27
	v_lshlrev_b32_e32 v18, 2, v196
	v_mov_b64_e32 v[16:17], s[54:55]
	s_waitcnt lgkmcnt(0)
	v_mfma_f32_32x32x16_bf16 v[82:97], v[26:29], v[142:145], v[82:97]
	ds_read_b128 v[22:25], v30 offset:49152
	ds_read_b128 v[26:29], v30 offset:57344
	v_add_u32_e32 v228, 0, v19
	v_add_u32_e32 v19, s0, v195
	v_mov_b64_e32 v[4:5], s[42:43]
	v_mov_b64_e32 v[6:7], s[44:45]
	v_mov_b64_e32 v[8:9], s[46:47]
	v_mov_b64_e32 v[10:11], s[48:49]
	s_waitcnt vmcnt(7) lgkmcnt(1)
	v_mfma_f32_32x32x16_bf16 v[66:81], v[22:25], v[146:149], v[66:81]
	v_mov_b64_e32 v[12:13], s[50:51]
	v_mov_b64_e32 v[14:15], s[52:53]
	v_sub_u32_e32 v229, v19, v18
	v_mov_b64_e32 v[48:49], v[16:17]
	v_mov_b64_e32 v[64:65], v[16:17]
	s_mov_b32 s34, 3
	v_mov_b32_e32 v230, 0
	s_waitcnt lgkmcnt(0)
	v_mfma_f32_32x32x16_bf16 v[82:97], v[26:29], v[146:149], v[82:97]
	ds_read_b128 v[22:25], v31 offset:49152
	ds_read_b128 v[26:29], v31 offset:57344
	v_mov_b32_e32 v231, 0xf149f2ca
	s_movk_i32 s37, 0x7f
	s_mov_b64 s[22:23], s[64:65]
	s_mov_b64 s[42:43], s[62:63]
	v_mov_b64_e32 v[46:47], v[14:15]
	v_mov_b64_e32 v[44:45], v[12:13]
	s_waitcnt vmcnt(6) lgkmcnt(1)
	v_mfma_f32_32x32x16_bf16 v[66:81], v[22:25], v[150:153], v[66:81]
	v_mov_b64_e32 v[42:43], v[10:11]
	v_mov_b64_e32 v[40:41], v[8:9]
	v_mov_b64_e32 v[38:39], v[6:7]
	v_mov_b64_e32 v[36:37], v[4:5]
	v_mov_b64_e32 v[34:35], v[2:3]
	v_mov_b64_e32 v[62:63], v[14:15]
	v_mov_b64_e32 v[60:61], v[12:13]
	s_waitcnt lgkmcnt(0)
	v_mfma_f32_32x32x16_bf16 v[82:97], v[26:29], v[150:153], v[82:97]
	ds_read_b128 v[22:25], v32 offset:49152
	ds_read_b128 v[26:29], v32 offset:57344
	v_mov_b64_e32 v[58:59], v[10:11]
	v_mov_b64_e32 v[56:57], v[8:9]
	v_mov_b64_e32 v[54:55], v[6:7]
	v_mov_b64_e32 v[52:53], v[4:5]
	v_mov_b64_e32 v[50:51], v[2:3]
	s_waitcnt vmcnt(5) lgkmcnt(1)
	v_mfma_f32_32x32x16_bf16 v[66:81], v[22:25], v[154:157], v[66:81]
	s_waitcnt lgkmcnt(0)
	v_mfma_f32_32x32x16_bf16 v[82:97], v[26:29], v[154:157], v[82:97]
	ds_read_b128 v[22:25], v33 offset:49152
	ds_read_b128 v[26:29], v33 offset:57344
	s_waitcnt vmcnt(4) lgkmcnt(1)
	v_mfma_f32_32x32x16_bf16 v[66:81], v[22:25], v[158:161], v[66:81]
	v_add_u32_e32 v24, v225, v226
	s_waitcnt lgkmcnt(0)
	v_mfma_f32_32x32x16_bf16 v[82:97], v[26:29], v[158:161], v[82:97]
	ds_read_b128 v[20:23], v24
	ds_read_b128 v[24:27], v24 offset:4096
	s_waitcnt vmcnt(3) lgkmcnt(1)
	v_mfma_f32_32x32x16_bf16 v[66:81], v[20:23], v[162:165], v[66:81]
	s_waitcnt lgkmcnt(0)
	v_mfma_f32_32x32x16_bf16 v[82:97], v[24:27], v[162:165], v[82:97]
	v_add_u32_e32 v24, v225, v206
	ds_read_b128 v[20:23], v24
	ds_read_b128 v[24:27], v24 offset:4096
	s_waitcnt vmcnt(2) lgkmcnt(1)
	v_mfma_f32_32x32x16_bf16 v[66:81], v[20:23], v[166:169], v[66:81]
	s_waitcnt lgkmcnt(0)
	v_mfma_f32_32x32x16_bf16 v[82:97], v[24:27], v[166:169], v[82:97]
	v_add_u32_e32 v24, v225, v208
	ds_read_b128 v[20:23], v24
	ds_read_b128 v[24:27], v24 offset:4096
	s_waitcnt vmcnt(1) lgkmcnt(1)
	v_mfma_f32_32x32x16_bf16 v[66:81], v[20:23], v[170:173], v[66:81]
	s_waitcnt lgkmcnt(0)
	v_mfma_f32_32x32x16_bf16 v[82:97], v[24:27], v[170:173], v[82:97]
	v_add_u32_e32 v24, v225, v223
	ds_read_b128 v[20:23], v24
	ds_read_b128 v[24:27], v24 offset:4096
	s_waitcnt vmcnt(0) lgkmcnt(1)
	v_mfma_f32_32x32x16_bf16 v[66:81], v[20:23], v[174:177], v[66:81]
	s_waitcnt lgkmcnt(0)
	v_mfma_f32_32x32x16_bf16 v[82:97], v[24:27], v[174:177], v[82:97]
	v_mov_b64_e32 v[32:33], v[16:17]
	v_mov_b64_e32 v[30:31], v[14:15]
	v_mov_b64_e32 v[28:29], v[12:13]
	v_mov_b64_e32 v[26:27], v[10:11]
	v_mov_b64_e32 v[24:25], v[8:9]
	v_mov_b64_e32 v[22:23], v[6:7]
	v_mov_b64_e32 v[20:21], v[4:5]
	v_mov_b64_e32 v[18:19], v[2:3]

.LBB0_946:
	s_lshl_b32 s50, s0, 14
	s_add_i32 s1, s50, 0
	v_add_u32_e32 v210, s1, v202
	ds_read_b128 v[98:101], v210 offset:49152
	ds_read_b128 v[102:105], v210 offset:57344
	v_xor_b32_e32 v210, 0x80, v210
	v_max_f32_e32 v186, v67, v67
	v_max_f32_e32 v187, v66, v66
	v_max_f32_e32 v186, v187, v186
	s_waitcnt lgkmcnt(1)
	v_mfma_f32_32x32x16_bf16 v[114:129], v[98:101], v[130:133], 0
	v_add_u32_e32 v212, s1, v207
	v_max3_f32 v186, v186, v68, v69
	ds_read_b128 v[178:181], v212 offset:49152
	ds_read_b128 v[182:185], v212 offset:57344
	v_xor_b32_e32 v212, 0x80, v212
	v_max3_f32 v186, v186, v70, v71
	v_max3_f32 v186, v186, v72, v73
	v_max3_f32 v186, v186, v74, v75
	v_max3_f32 v186, v186, v76, v77
	s_waitcnt lgkmcnt(2)
	v_mfma_f32_32x32x16_bf16 v[98:113], v[102:105], v[130:133], 0
	v_max3_f32 v186, v186, v78, v79
	v_lshl_add_u32 v211, s0, 13, v225
	v_max3_f32 v213, v186, v80, v81
	s_waitcnt lgkmcnt(1)
	v_mfma_f32_32x32x16_bf16 v[114:129], v[178:181], v[134:137], v[114:129]
	v_max3_f32 v178, v213, v82, v83
	v_max3_f32 v178, v178, v84, v85
	v_max3_f32 v178, v178, v86, v87
	v_max3_f32 v178, v178, v88, v89
	v_max3_f32 v178, v178, v90, v91
	v_max3_f32 v178, v178, v92, v93
	v_max3_f32 v178, v178, v94, v95
	v_max3_f32 v178, v178, v96, v97
	v_mov_b32_e32 v179, v178
	s_nop 1
	v_permlane32_swap_b32_e32 v178, v179
	v_max_f32_e32 v179, v179, v179
	v_max_f32_e32 v178, v178, v178
	v_max_f32_e32 v178, v178, v179
	v_sub_f32_e32 v179, v178, v231
	v_mul_f32_e32 v179, 0x3d93cd3a, v179
	v_cmp_ge_f32_e32 vcc, s36, v179
	s_cmp_eq_u64 vcc, exec
	v_max_f32_e32 v179, v231, v231
	s_waitcnt lgkmcnt(0)
	v_mfma_f32_32x32x16_bf16 v[98:113], v[182:185], v[134:137], v[98:113]
	s_cselect_b64 vcc, -1, 0
	v_max_f32_e32 v178, v179, v178
	v_cndmask_b32_e32 v232, v178, v231, vcc
	v_add_u32_e32 v218, s1, v209
	v_sub_f32_e32 v178, v231, v232
	ds_read_b128 v[186:189], v218 offset:49152
	ds_read_b128 v[190:193], v218 offset:57344
	v_xor_b32_e32 v218, 0x80, v218
	v_mul_f32_e32 v178, 0x3dd53b94, v178
	v_exp_f32_e32 v231, v178
	v_mul_f32_e32 v213, 0xbdd53b94, v232
	v_fmamk_f32 v66, v66, 0x3dd53b94, v213
	s_waitcnt lgkmcnt(1)
	v_mfma_f32_32x32x16_bf16 v[114:129], v[186:189], v[138:141], v[114:129]
	v_exp_f32_e32 v66, v66
	v_fmamk_f32 v82, v82, 0x3dd53b94, v213
	v_add_u32_e32 v219, s1, v224
	v_exp_f32_e32 v82, v82
	v_fmamk_f32 v67, v67, 0x3dd53b94, v213
	ds_read_b128 v[178:181], v219 offset:49152
	ds_read_b128 v[182:185], v219 offset:57344
	v_xor_b32_e32 v219, 0x80, v219
	v_exp_f32_e32 v67, v67
	s_waitcnt lgkmcnt(2)
	v_mfma_f32_32x32x16_bf16 v[98:113], v[190:193], v[138:141], v[98:113]
	v_fmamk_f32 v83, v83, 0x3dd53b94, v213
	v_exp_f32_e32 v83, v83
	v_add_f32_e32 v186, 0, v66
	v_add_f32_e32 v186, v82, v186
	v_add_f32_e32 v186, v67, v186
	v_add_f32_e32 v220, v83, v186
	v_fmamk_f32 v68, v68, 0x3dd53b94, v213
	s_waitcnt lgkmcnt(1)
	v_mfma_f32_32x32x16_bf16 v[114:129], v[178:181], v[142:145], v[114:129]
	v_exp_f32_e32 v68, v68
	v_fmamk_f32 v84, v84, 0x3dd53b94, v213
	v_exp_f32_e32 v84, v84
	v_fmamk_f32 v69, v69, 0x3dd53b94, v213
	ds_read_b128 v[186:189], v210 offset:49152
	ds_read_b128 v[190:193], v210 offset:57344
	v_exp_f32_e32 v69, v69
	v_fmamk_f32 v85, v85, 0x3dd53b94, v213
	s_waitcnt lgkmcnt(2)
	v_mfma_f32_32x32x16_bf16 v[98:113], v[182:185], v[142:145], v[98:113]
	v_exp_f32_e32 v85, v85
	v_add_f32_e32 v178, v68, v220
	v_add_f32_e32 v178, v84, v178
	v_add_f32_e32 v178, v69, v178
	v_add_f32_e32 v210, v85, v178
	v_fmamk_f32 v70, v70, 0x3dd53b94, v213
	s_waitcnt lgkmcnt(1)
	v_mfma_f32_32x32x16_bf16 v[114:129], v[186:189], v[146:149], v[114:129]
	v_exp_f32_e32 v70, v70
	v_fmamk_f32 v86, v86, 0x3dd53b94, v213
	v_exp_f32_e32 v86, v86
	v_fmamk_f32 v71, v71, 0x3dd53b94, v213
	ds_read_b128 v[178:181], v212 offset:49152
	ds_read_b128 v[182:185], v212 offset:57344
	v_exp_f32_e32 v71, v71
	v_fmamk_f32 v87, v87, 0x3dd53b94, v213
	s_waitcnt lgkmcnt(2)
	v_mfma_f32_32x32x16_bf16 v[98:113], v[190:193], v[146:149], v[98:113]
	v_exp_f32_e32 v87, v87
	v_add_f32_e32 v186, v70, v210
	v_add_f32_e32 v186, v86, v186
	v_add_f32_e32 v186, v71, v186
	v_add_f32_e32 v210, v87, v186
	v_fmamk_f32 v72, v72, 0x3dd53b94, v213
	s_waitcnt lgkmcnt(1)
	v_mfma_f32_32x32x16_bf16 v[114:129], v[178:181], v[150:153], v[114:129]
	v_exp_f32_e32 v72, v72
	v_fmamk_f32 v88, v88, 0x3dd53b94, v213
	v_exp_f32_e32 v88, v88
	v_fmamk_f32 v73, v73, 0x3dd53b94, v213
	ds_read_b128 v[186:189], v218 offset:49152
	ds_read_b128 v[190:193], v218 offset:57344
	v_exp_f32_e32 v73, v73
	v_fmamk_f32 v89, v89, 0x3dd53b94, v213
	s_waitcnt lgkmcnt(2)
	v_mfma_f32_32x32x16_bf16 v[98:113], v[182:185], v[150:153], v[98:113]
	v_exp_f32_e32 v89, v89
	v_add_f32_e32 v178, v72, v210
	v_add_f32_e32 v178, v88, v178
	v_add_f32_e32 v178, v73, v178
	v_add_f32_e32 v210, v89, v178
	v_fmamk_f32 v74, v74, 0x3dd53b94, v213
	v_exp_f32_e32 v74, v74
	v_fmamk_f32 v90, v90, 0x3dd53b94, v213
	s_waitcnt lgkmcnt(1)
	v_mfma_f32_32x32x16_bf16 v[114:129], v[186:189], v[154:157], v[114:129]
	v_exp_f32_e32 v90, v90
	v_fmamk_f32 v75, v75, 0x3dd53b94, v213
	v_exp_f32_e32 v75, v75
	v_fmamk_f32 v91, v91, 0x3dd53b94, v213
	ds_read_b128 v[178:181], v219 offset:49152
	ds_read_b128 v[182:185], v219 offset:57344
	v_exp_f32_e32 v91, v91
	v_add_f32_e32 v186, v74, v210
	s_waitcnt lgkmcnt(2)
	v_mfma_f32_32x32x16_bf16 v[98:113], v[190:193], v[154:157], v[98:113]
	v_add_f32_e32 v186, v90, v186
	v_add_f32_e32 v186, v75, v186
	v_add_f32_e32 v190, v91, v186
	v_fmamk_f32 v76, v76, 0x3dd53b94, v213
	v_exp_f32_e32 v76, v76
	v_fmamk_f32 v92, v92, 0x3dd53b94, v213
	s_waitcnt lgkmcnt(1)
	v_mfma_f32_32x32x16_bf16 v[114:129], v[178:181], v[158:161], v[114:129]
	v_exp_f32_e32 v92, v92
	v_fmamk_f32 v77, v77, 0x3dd53b94, v213
	v_add_u32_e32 v186, v211, v226
	v_exp_f32_e32 v77, v77
	v_fmamk_f32 v93, v93, 0x3dd53b94, v213
	ds_read_b128 v[178:181], v186
	ds_read_b128 v[186:189], v186 offset:4096
	v_exp_f32_e32 v93, v93
	s_waitcnt lgkmcnt(2)
	v_mfma_f32_32x32x16_bf16 v[98:113], v[182:185], v[158:161], v[98:113]
	v_add_f32_e32 v190, v76, v190
	v_add_f32_e32 v190, v92, v190
	v_add_f32_e32 v182, v77, v190
	v_add_f32_e32 v190, v93, v182
	v_fmamk_f32 v78, v78, 0x3dd53b94, v213
	v_exp_f32_e32 v78, v78
	v_fmamk_f32 v94, v94, 0x3dd53b94, v213
	s_waitcnt lgkmcnt(1)
	v_mfma_f32_32x32x16_bf16 v[114:129], v[178:181], v[162:165], v[114:129]
	v_exp_f32_e32 v94, v94
	v_fmamk_f32 v79, v79, 0x3dd53b94, v213
	v_add_u32_e32 v182, v211, v206
	v_exp_f32_e32 v79, v79
	v_fmamk_f32 v95, v95, 0x3dd53b94, v213
	ds_read_b128 v[178:181], v182
	ds_read_b128 v[182:185], v182 offset:4096
	v_exp_f32_e32 v95, v95
	s_waitcnt lgkmcnt(2)
	v_mfma_f32_32x32x16_bf16 v[98:113], v[186:189], v[162:165], v[98:113]
	v_add_f32_e32 v190, v78, v190
	v_add_f32_e32 v190, v94, v190
	v_add_f32_e32 v186, v79, v190
	v_add_f32_e32 v190, v95, v186
	v_fmamk_f32 v80, v80, 0x3dd53b94, v213
	v_exp_f32_e32 v80, v80
	v_fmamk_f32 v96, v96, 0x3dd53b94, v213
	s_waitcnt lgkmcnt(1)
	v_mfma_f32_32x32x16_bf16 v[114:129], v[178:181], v[166:169], v[114:129]
	v_exp_f32_e32 v96, v96
	v_fmamk_f32 v81, v81, 0x3dd53b94, v213
	v_add_u32_e32 v186, v211, v208
	v_exp_f32_e32 v81, v81
	v_fmac_f32_e32 v213, 0x3dd53b94, v97
	ds_read_b128 v[178:181], v186
	ds_read_b128 v[186:189], v186 offset:4096
	v_exp_f32_e32 v97, v213
	s_waitcnt lgkmcnt(2)
	v_mfma_f32_32x32x16_bf16 v[98:113], v[182:185], v[166:169], v[98:113]
	v_add_f32_e32 v190, v80, v190
	v_add_f32_e32 v190, v96, v190
	v_add_f32_e32 v182, v81, v190
	v_add_f32_e32 v233, v97, v182
	s_waitcnt lgkmcnt(1)
	v_mfma_f32_32x32x16_bf16 v[114:129], v[178:181], v[170:173], v[114:129]
	v_add_u32_e32 v182, v211, v223
	ds_read_b128 v[190:193], v182
	ds_read_b128 v[236:239], v182 offset:4096
	v_mov_b32_e32 v234, v233
	v_cvt_pk_bf16_f32 v178, v66, v67
	v_cvt_pk_bf16_f32 v179, v68, v69
	v_cvt_pk_bf16_f32 v180, v70, v71
	v_cvt_pk_bf16_f32 v181, v72, v73
	s_waitcnt lgkmcnt(2)
	v_mfma_f32_32x32x16_bf16 v[98:113], v[186:189], v[170:173], v[98:113]
	v_cvt_pk_bf16_f32 v182, v74, v75
	v_cvt_pk_bf16_f32 v183, v76, v77
	v_cvt_pk_bf16_f32 v184, v78, v79
	v_cvt_pk_bf16_f32 v185, v80, v81
	v_permlane32_swap_b32_e32 v233, v234
	v_permlane32_swap_b32_e32 v178, v180
	v_permlane32_swap_b32_e32 v179, v181
	v_permlane32_swap_b32_e32 v182, v184
	v_permlane32_swap_b32_e32 v183, v185
	s_waitcnt lgkmcnt(1)
	v_mfma_f32_32x32x16_bf16 v[114:129], v[190:193], v[174:177], v[114:129]
	v_cvt_pk_bf16_f32 v186, v82, v83
	v_cvt_pk_bf16_f32 v187, v84, v85
	v_cvt_pk_bf16_f32 v188, v86, v87
	v_cvt_pk_bf16_f32 v189, v88, v89
	v_cvt_pk_bf16_f32 v190, v90, v91
	v_cvt_pk_bf16_f32 v191, v92, v93
	v_cvt_pk_bf16_f32 v192, v94, v95
	s_waitcnt lgkmcnt(0)
	v_mfma_f32_32x32x16_bf16 v[98:113], v[236:239], v[174:177], v[98:113]
	v_cvt_pk_bf16_f32 v193, v96, v97
	v_permlane32_swap_b32_e32 v186, v188
	v_permlane32_swap_b32_e32 v187, v189
	v_permlane32_swap_b32_e32 v190, v192
	v_permlane32_swap_b32_e32 v191, v193
	v_cmp_gt_f32_e32 vcc, 1.0, v231
	s_cbranch_vccz .LBB0_950
	s_and_saveexec_b64 s[46:47], s[2:3]
	ds_write_b32 v227, v231 offset:128
	s_or_b64 exec, exec, s[46:47]
	s_waitcnt lgkmcnt(0)
	ds_read_b128 v[236:239], v1 offset:224
	ds_read_b128 v[240:243], v1 offset:192
	ds_read_b128 v[244:247], v1 offset:160
	ds_read_b128 v[218:221], v1 offset:128
	s_waitcnt lgkmcnt(3)
	v_pk_mul_f32 v[64:65], v[64:65], v[238:239]
	s_waitcnt lgkmcnt(2)
	v_pk_mul_f32 v[60:61], v[60:61], v[242:243]
	s_waitcnt lgkmcnt(1)
	v_pk_mul_f32 v[56:57], v[56:57], v[246:247]
	s_waitcnt lgkmcnt(0)
	v_pk_mul_f32 v[52:53], v[52:53], v[220:221]
	v_pk_mul_f32 v[62:63], v[62:63], v[236:237]
	v_pk_mul_f32 v[58:59], v[58:59], v[240:241]
	v_pk_mul_f32 v[54:55], v[54:55], v[244:245]
	v_pk_mul_f32 v[50:51], v[50:51], v[218:219]
	v_pk_mul_f32 v[48:49], v[48:49], v[238:239]
	v_pk_mul_f32 v[44:45], v[44:45], v[242:243]
	v_pk_mul_f32 v[40:41], v[40:41], v[246:247]
	v_pk_mul_f32 v[36:37], v[36:37], v[220:221]
	v_pk_mul_f32 v[46:47], v[46:47], v[236:237]
	v_pk_mul_f32 v[42:43], v[42:43], v[240:241]
	v_pk_mul_f32 v[38:39], v[38:39], v[244:245]
	v_pk_mul_f32 v[34:35], v[34:35], v[218:219]
	v_pk_mul_f32 v[32:33], v[32:33], v[238:239]
	v_pk_mul_f32 v[28:29], v[28:29], v[242:243]
	v_pk_mul_f32 v[24:25], v[24:25], v[246:247]
	v_pk_mul_f32 v[20:21], v[20:21], v[220:221]
	v_pk_mul_f32 v[30:31], v[30:31], v[236:237]
	v_pk_mul_f32 v[26:27], v[26:27], v[240:241]
	v_pk_mul_f32 v[22:23], v[22:23], v[244:245]
	v_pk_mul_f32 v[18:19], v[18:19], v[218:219]
	v_pk_mul_f32 v[16:17], v[16:17], v[238:239]
	v_pk_mul_f32 v[12:13], v[12:13], v[242:243]
	v_pk_mul_f32 v[8:9], v[8:9], v[246:247]
	v_pk_mul_f32 v[4:5], v[4:5], v[220:221]
	v_pk_mul_f32 v[14:15], v[14:15], v[236:237]
	v_pk_mul_f32 v[10:11], v[10:11], v[240:241]
	v_pk_mul_f32 v[6:7], v[6:7], v[244:245]
	v_pk_mul_f32 v[2:3], v[2:3], v[218:219]

.LBB0_958:
	s_lshl_b32 s0, s48, 14
	s_add_i32 s0, s0, 0
	v_add_u32_e32 v210, s0, v202
	ds_read_b128 v[66:69], v210 offset:49152
	ds_read_b128 v[82:85], v210 offset:57344
	v_xor_b32_e32 v210, 0x80, v210
	v_max_f32_e32 v86, v237, v236
	v_max3_f32 v86, v86, v116, v117
	v_max3_f32 v86, v86, v118, v119
	v_max3_f32 v186, v86, v120, v121
	v_add_u32_e32 v212, s0, v207
	ds_read_b128 v[178:181], v212 offset:49152
	ds_read_b128 v[182:185], v212 offset:57344
	v_xor_b32_e32 v212, 0x80, v212
	v_max3_f32 v186, v186, v122, v123
	s_waitcnt lgkmcnt(3)
	v_mfma_f32_32x32x16_bf16 v[66:81], v[66:69], v[130:133], 0
	v_max3_f32 v186, v186, v124, v125
	v_max3_f32 v186, v186, v126, v127
	v_lshl_add_u32 v211, s48, 13, v225
	v_max3_f32 v213, v186, v128, v129
	s_waitcnt lgkmcnt(2)
	v_mfma_f32_32x32x16_bf16 v[82:97], v[82:85], v[130:133], 0
	s_waitcnt lgkmcnt(1)
	v_mfma_f32_32x32x16_bf16 v[66:81], v[178:181], v[134:137], v[66:81]
	v_max3_f32 v178, v213, v98, v99
	v_max3_f32 v178, v178, v100, v101
	v_max3_f32 v178, v178, v102, v103
	v_max3_f32 v178, v178, v104, v105
	v_max3_f32 v178, v178, v106, v107
	v_max3_f32 v178, v178, v108, v109
	v_max3_f32 v178, v178, v110, v111
	v_max3_f32 v178, v178, v112, v113
	v_mov_b32_e32 v179, v178
	s_nop 1
	v_permlane32_swap_b32_e32 v178, v179
	v_max_f32_e32 v179, v179, v179
	v_max_f32_e32 v178, v178, v178
	v_max_f32_e32 v178, v178, v179
	v_sub_f32_e32 v179, v178, v232
	v_mul_f32_e32 v179, 0x3d93cd3a, v179
	v_cmp_ge_f32_e32 vcc, s36, v179
	s_cmp_eq_u64 vcc, exec
	s_waitcnt lgkmcnt(0)
	v_mfma_f32_32x32x16_bf16 v[82:97], v[182:185], v[134:137], v[82:97]
	s_cselect_b64 vcc, -1, 0
	v_max_f32_e32 v178, v235, v178
	v_cndmask_b32_e32 v231, v178, v232, vcc
	v_add_u32_e32 v218, s0, v209
	v_sub_f32_e32 v178, v232, v231
	ds_read_b128 v[186:189], v218 offset:49152
	ds_read_b128 v[190:193], v218 offset:57344
	v_xor_b32_e32 v218, 0x80, v218
	v_mul_f32_e32 v178, 0x3dd53b94, v178
	v_exp_f32_e32 v234, v178
	v_mul_f32_e32 v213, 0xbdd53b94, v231
	v_fmamk_f32 v114, v114, 0x3dd53b94, v213
	s_waitcnt lgkmcnt(1)
	v_mfma_f32_32x32x16_bf16 v[66:81], v[186:189], v[138:141], v[66:81]
	v_exp_f32_e32 v220, v114
	v_fmamk_f32 v98, v98, 0x3dd53b94, v213
	v_add_u32_e32 v219, s0, v224
	v_exp_f32_e32 v221, v98
	v_fmamk_f32 v114, v115, 0x3dd53b94, v213
	ds_read_b128 v[178:181], v219 offset:49152
	ds_read_b128 v[182:185], v219 offset:57344
	v_xor_b32_e32 v219, 0x80, v219
	v_exp_f32_e32 v232, v114
	s_waitcnt lgkmcnt(2)
	v_mfma_f32_32x32x16_bf16 v[82:97], v[190:193], v[138:141], v[82:97]
	v_fmamk_f32 v99, v99, 0x3dd53b94, v213
	v_exp_f32_e32 v235, v99
	v_add_f32_e32 v98, 0, v220
	v_add_f32_e32 v98, v221, v98
	v_add_f32_e32 v98, v232, v98
	v_add_f32_e32 v98, v235, v98
	v_fmamk_f32 v99, v116, 0x3dd53b94, v213
	ds_read_b128 v[186:189], v210 offset:49152
	ds_read_b128 v[190:193], v210 offset:57344
	v_exp_f32_e32 v210, v99
	v_fmamk_f32 v99, v100, 0x3dd53b94, v213
	s_waitcnt lgkmcnt(3)
	v_mfma_f32_32x32x16_bf16 v[66:81], v[178:181], v[142:145], v[66:81]
	v_exp_f32_e32 v236, v99
	v_fmamk_f32 v99, v117, 0x3dd53b94, v213
	v_exp_f32_e32 v237, v99
	v_fmamk_f32 v99, v101, 0x3dd53b94, v213
	v_exp_f32_e32 v238, v99
	v_add_f32_e32 v98, v210, v98
	v_add_f32_e32 v98, v236, v98
	s_waitcnt lgkmcnt(2)
	v_mfma_f32_32x32x16_bf16 v[82:97], v[182:185], v[142:145], v[82:97]
	v_add_f32_e32 v98, v237, v98
	v_add_f32_e32 v178, v238, v98
	v_fmamk_f32 v118, v118, 0x3dd53b94, v213
	s_waitcnt lgkmcnt(1)
	v_mfma_f32_32x32x16_bf16 v[66:81], v[186:189], v[146:149], v[66:81]
	v_exp_f32_e32 v118, v118
	v_fmamk_f32 v102, v102, 0x3dd53b94, v213
	ds_read_b128 v[98:101], v212 offset:49152
	ds_read_b128 v[114:117], v212 offset:57344
	v_exp_f32_e32 v212, v102
	v_fmamk_f32 v119, v119, 0x3dd53b94, v213
	v_exp_f32_e32 v119, v119
	v_fmamk_f32 v103, v103, 0x3dd53b94, v213
	s_waitcnt lgkmcnt(2)
	v_mfma_f32_32x32x16_bf16 v[82:97], v[190:193], v[146:149], v[82:97]
	v_exp_f32_e32 v188, v103
	v_add_f32_e32 v102, v118, v178
	v_add_f32_e32 v102, v212, v102
	v_add_f32_e32 v102, v119, v102
	v_add_f32_e32 v102, v188, v102
	v_fmamk_f32 v103, v120, 0x3dd53b94, v213
	s_waitcnt lgkmcnt(1)
	v_mfma_f32_32x32x16_bf16 v[66:81], v[98:101], v[150:153], v[66:81]
	v_exp_f32_e32 v120, v103
	v_fmamk_f32 v103, v104, 0x3dd53b94, v213
	v_exp_f32_e32 v189, v103
	v_fmamk_f32 v99, v121, 0x3dd53b94, v213
	ds_read_b128 v[178:181], v218 offset:49152
	ds_read_b128 v[182:185], v218 offset:57344
	v_exp_f32_e32 v121, v99
	v_fmamk_f32 v99, v105, 0x3dd53b94, v213
	s_waitcnt lgkmcnt(2)
	v_mfma_f32_32x32x16_bf16 v[82:97], v[114:117], v[150:153], v[82:97]
	v_exp_f32_e32 v190, v99
	v_add_f32_e32 v98, v120, v102
	v_add_f32_e32 v98, v189, v98
	v_add_f32_e32 v98, v121, v98
	v_add_f32_e32 v114, v190, v98
	v_fmamk_f32 v115, v122, 0x3dd53b94, v213
	v_exp_f32_e32 v122, v115
	s_waitcnt lgkmcnt(1)
	v_mfma_f32_32x32x16_bf16 v[66:81], v[178:181], v[154:157], v[66:81]
	v_fmamk_f32 v106, v106, 0x3dd53b94, v213
	v_exp_f32_e32 v191, v106
	v_add_f32_e32 v106, v122, v114
	v_fmamk_f32 v114, v123, 0x3dd53b94, v213
	ds_read_b128 v[98:101], v219 offset:49152
	ds_read_b128 v[102:105], v219 offset:57344
	v_exp_f32_e32 v123, v114
	v_fmamk_f32 v107, v107, 0x3dd53b94, v213
	s_waitcnt lgkmcnt(2)
	v_mfma_f32_32x32x16_bf16 v[82:97], v[182:185], v[154:157], v[82:97]
	v_exp_f32_e32 v192, v107
	v_add_f32_e32 v106, v191, v106
	v_add_f32_e32 v106, v123, v106
	v_add_f32_e32 v106, v192, v106
	v_fmamk_f32 v114, v124, 0x3dd53b94, v213
	s_waitcnt lgkmcnt(1)
	v_mfma_f32_32x32x16_bf16 v[66:81], v[98:101], v[158:161], v[66:81]
	v_add_u32_e32 v107, v211, v226
	v_exp_f32_e32 v124, v114
	v_fmamk_f32 v108, v108, 0x3dd53b94, v213
	v_exp_f32_e32 v193, v108
	ds_read_b128 v[98:101], v107
	ds_read_b128 v[114:117], v107 offset:4096
	v_fmamk_f32 v107, v125, 0x3dd53b94, v213
	v_exp_f32_e32 v125, v107
	s_waitcnt lgkmcnt(2)
	v_mfma_f32_32x32x16_bf16 v[82:97], v[102:105], v[158:161], v[82:97]
	v_fmamk_f32 v107, v109, 0x3dd53b94, v213
	v_exp_f32_e32 v218, v107
	v_add_f32_e32 v106, v124, v106
	v_add_f32_e32 v106, v193, v106
	v_add_f32_e32 v102, v125, v106
	v_add_f32_e32 v106, v218, v102
	v_fmamk_f32 v103, v126, 0x3dd53b94, v213
	s_waitcnt lgkmcnt(1)
	v_mfma_f32_32x32x16_bf16 v[66:81], v[98:101], v[162:165], v[66:81]
	v_exp_f32_e32 v126, v103
	v_fmamk_f32 v103, v110, 0x3dd53b94, v213
	v_add_u32_e32 v102, v211, v206
	v_exp_f32_e32 v219, v103
	v_fmamk_f32 v107, v127, 0x3dd53b94, v213
	ds_read_b128 v[98:101], v102
	ds_read_b128 v[102:105], v102 offset:4096
	v_exp_f32_e32 v127, v107
	s_waitcnt lgkmcnt(2)
	v_mfma_f32_32x32x16_bf16 v[82:97], v[114:117], v[162:165], v[82:97]
	v_fmamk_f32 v107, v111, 0x3dd53b94, v213
	v_exp_f32_e32 v239, v107
	v_add_f32_e32 v106, v126, v106
	v_add_f32_e32 v106, v219, v106
	v_add_f32_e32 v106, v127, v106
	v_add_f32_e32 v110, v239, v106
	v_fmamk_f32 v107, v128, 0x3dd53b94, v213
	s_waitcnt lgkmcnt(1)
	v_mfma_f32_32x32x16_bf16 v[66:81], v[98:101], v[166:169], v[66:81]
	v_exp_f32_e32 v114, v107
	v_fmamk_f32 v107, v112, 0x3dd53b94, v213
	v_add_u32_e32 v106, v211, v208
	v_exp_f32_e32 v115, v107
	v_fmamk_f32 v111, v129, 0x3dd53b94, v213
	ds_read_b128 v[98:101], v106
	ds_read_b128 v[106:109], v106 offset:4096
	v_exp_f32_e32 v116, v111
	s_waitcnt lgkmcnt(2)
	v_mfma_f32_32x32x16_bf16 v[82:97], v[102:105], v[166:169], v[82:97]
	v_fmac_f32_e32 v213, 0x3dd53b94, v113
	v_exp_f32_e32 v117, v213
	v_add_f32_e32 v110, v114, v110
	v_add_f32_e32 v110, v115, v110
	v_add_f32_e32 v102, v116, v110
	v_add_f32_e32 v128, v117, v102
	s_waitcnt lgkmcnt(1)
	v_mfma_f32_32x32x16_bf16 v[66:81], v[98:101], v[170:173], v[66:81]
	v_add_u32_e32 v110, v211, v223
	ds_read_b128 v[102:105], v110
	ds_read_b128 v[110:113], v110 offset:4096
	v_mov_b32_e32 v129, v128
	s_nop 1
	v_permlane32_swap_b32_e32 v128, v129
	v_add_f32_e32 v230, v128, v129
	v_cvt_pk_bf16_f32 v178, v220, v232
	s_waitcnt lgkmcnt(2)
	v_mfma_f32_32x32x16_bf16 v[82:97], v[106:109], v[170:173], v[82:97]
	v_cvt_pk_bf16_f32 v179, v210, v237
	v_cvt_pk_bf16_f32 v180, v118, v119
	v_cvt_pk_bf16_f32 v181, v120, v121
	v_cvt_pk_bf16_f32 v182, v122, v123
	v_cvt_pk_bf16_f32 v183, v124, v125
	v_cvt_pk_bf16_f32 v184, v126, v127
	v_cvt_pk_bf16_f32 v185, v114, v116
	v_fmac_f32_e32 v230, v233, v234
	v_permlane32_swap_b32_e32 v178, v180
	v_permlane32_swap_b32_e32 v179, v181
	v_permlane32_swap_b32_e32 v182, v184
	v_permlane32_swap_b32_e32 v183, v185
	s_waitcnt lgkmcnt(1)
	v_mfma_f32_32x32x16_bf16 v[66:81], v[102:105], v[174:177], v[66:81]
	v_cvt_pk_bf16_f32 v186, v221, v235
	v_cvt_pk_bf16_f32 v187, v236, v238
	v_cvt_pk_bf16_f32 v188, v212, v188
	v_cvt_pk_bf16_f32 v189, v189, v190
	v_cvt_pk_bf16_f32 v190, v191, v192
	v_cvt_pk_bf16_f32 v191, v193, v218
	v_cvt_pk_bf16_f32 v192, v219, v239
	s_waitcnt lgkmcnt(0)
	v_mfma_f32_32x32x16_bf16 v[82:97], v[110:113], v[174:177], v[82:97]
	v_cvt_pk_bf16_f32 v193, v115, v117
	v_permlane32_swap_b32_e32 v186, v188
	v_permlane32_swap_b32_e32 v187, v189
	v_permlane32_swap_b32_e32 v190, v192
	v_permlane32_swap_b32_e32 v191, v193
	v_cmp_gt_f32_e32 vcc, 1.0, v234
	s_cbranch_vccz .LBB0_962
